# prep tail (MoBA block means): 4 serialized load/accumulate iterations unrolled with all 16 loads in flight
# baseline (speedup 1.0000x reference)
.LBB0_348:
	v_lshl_add_u64 v[8:9], v[4:5], 0, s[8:9]
	v_add_co_u32_e32 v10, vcc, 0x37c82000, v8
	s_add_u32 s8, s8, 0xd000
	s_nop 0
	v_addc_co_u32_e32 v11, vcc, 0, v9, vcc
	v_add_co_u32_e32 v12, vcc, s12, v8
	global_load_dwordx2 v[10:11], v[10:11], off offset:576
	s_nop 0
	v_addc_co_u32_e32 v13, vcc, 0, v9, vcc
	v_add_co_u32_e32 v14, vcc, s13, v8
	global_load_dwordx2 v[12:13], v[12:13], off offset:1600
	s_nop 0
	v_addc_co_u32_e32 v15, vcc, 0, v9, vcc
	v_add_co_u32_e32 v8, vcc, s14, v8
	global_load_dwordx2 v[14:15], v[14:15], off offset:2624
	s_nop 0
	v_addc_co_u32_e32 v9, vcc, 0, v9, vcc
	global_load_dwordx2 v[8:9], v[8:9], off offset:3648
	s_addc_u32 s9, s9, 0
	s_cmp_eq_u32 s8, 0x34000
	v_lshl_add_u64 v[18:19], v[4:5], 0, s[8:9]
	v_add_co_u32_e32 v20, vcc, 0x37c82000, v18
	s_add_u32 s8, s8, 0xd000
	s_nop 0
	v_addc_co_u32_e32 v21, vcc, 0, v19, vcc
	v_add_co_u32_e32 v22, vcc, s12, v18
	global_load_dwordx2 v[20:21], v[20:21], off offset:576
	s_nop 0
	v_addc_co_u32_e32 v23, vcc, 0, v19, vcc
	v_add_co_u32_e32 v24, vcc, s13, v18
	global_load_dwordx2 v[22:23], v[22:23], off offset:1600
	s_nop 0
	v_addc_co_u32_e32 v25, vcc, 0, v19, vcc
	v_add_co_u32_e32 v18, vcc, s14, v18
	global_load_dwordx2 v[24:25], v[24:25], off offset:2624
	s_nop 0
	v_addc_co_u32_e32 v19, vcc, 0, v19, vcc
	global_load_dwordx2 v[18:19], v[18:19], off offset:3648
	s_addc_u32 s9, s9, 0
	s_cmp_eq_u32 s8, 0x34000
	v_lshl_add_u64 v[28:29], v[4:5], 0, s[8:9]
	v_add_co_u32_e32 v30, vcc, 0x37c82000, v28
	s_add_u32 s8, s8, 0xd000
	s_nop 0
	v_addc_co_u32_e32 v31, vcc, 0, v29, vcc
	v_add_co_u32_e32 v32, vcc, s12, v28
	global_load_dwordx2 v[30:31], v[30:31], off offset:576
	s_nop 0
	v_addc_co_u32_e32 v33, vcc, 0, v29, vcc
	v_add_co_u32_e32 v34, vcc, s13, v28
	global_load_dwordx2 v[32:33], v[32:33], off offset:1600
	s_nop 0
	v_addc_co_u32_e32 v35, vcc, 0, v29, vcc
	v_add_co_u32_e32 v28, vcc, s14, v28
	global_load_dwordx2 v[34:35], v[34:35], off offset:2624
	s_nop 0
	v_addc_co_u32_e32 v29, vcc, 0, v29, vcc
	global_load_dwordx2 v[28:29], v[28:29], off offset:3648
	s_addc_u32 s9, s9, 0
	s_cmp_eq_u32 s8, 0x34000
	v_lshl_add_u64 v[206:207], v[4:5], 0, s[8:9]
	v_add_co_u32_e32 v208, vcc, 0x37c82000, v206
	s_add_u32 s8, s8, 0xd000
	s_nop 0
	v_addc_co_u32_e32 v209, vcc, 0, v207, vcc
	v_add_co_u32_e32 v210, vcc, s12, v206
	global_load_dwordx2 v[208:209], v[208:209], off offset:576
	s_nop 0
	v_addc_co_u32_e32 v211, vcc, 0, v207, vcc
	v_add_co_u32_e32 v212, vcc, s13, v206
	global_load_dwordx2 v[210:211], v[210:211], off offset:1600
	s_nop 0
	v_addc_co_u32_e32 v213, vcc, 0, v207, vcc
	v_add_co_u32_e32 v206, vcc, s14, v206
	global_load_dwordx2 v[212:213], v[212:213], off offset:2624
	s_nop 0
	v_addc_co_u32_e32 v207, vcc, 0, v207, vcc
	global_load_dwordx2 v[206:207], v[206:207], off offset:3648
	s_addc_u32 s9, s9, 0
	s_cmp_eq_u32 s8, 0x34000
	s_waitcnt vmcnt(15)
	v_lshlrev_b32_e32 v16, 16, v10
	v_and_b32_e32 v17, 0xffff0000, v10
	v_lshlrev_b32_e32 v10, 16, v11
	v_and_b32_e32 v11, 0xffff0000, v11
	v_pk_add_f32 v[0:1], v[0:1], v[16:17]
	v_pk_add_f32 v[2:3], v[2:3], v[10:11]
	s_waitcnt vmcnt(14)
	v_lshlrev_b32_e32 v10, 16, v12
	v_and_b32_e32 v11, 0xffff0000, v12
	v_lshlrev_b32_e32 v12, 16, v13
	v_and_b32_e32 v13, 0xffff0000, v13
	v_pk_add_f32 v[0:1], v[0:1], v[10:11]
	v_pk_add_f32 v[2:3], v[2:3], v[12:13]
	s_waitcnt vmcnt(13)
	v_lshlrev_b32_e32 v10, 16, v14
	v_and_b32_e32 v11, 0xffff0000, v14
	v_lshlrev_b32_e32 v12, 16, v15
	v_and_b32_e32 v13, 0xffff0000, v15
	v_pk_add_f32 v[0:1], v[0:1], v[10:11]
	v_pk_add_f32 v[2:3], v[2:3], v[12:13]
	s_waitcnt vmcnt(12)
	v_lshlrev_b32_e32 v10, 16, v8
	v_and_b32_e32 v11, 0xffff0000, v8
	v_lshlrev_b32_e32 v8, 16, v9
	v_and_b32_e32 v9, 0xffff0000, v9
	v_pk_add_f32 v[0:1], v[0:1], v[10:11]
	v_pk_add_f32 v[2:3], v[2:3], v[8:9]
	s_waitcnt vmcnt(11)
	v_lshlrev_b32_e32 v16, 16, v20
	v_and_b32_e32 v17, 0xffff0000, v20
	v_lshlrev_b32_e32 v20, 16, v21
	v_and_b32_e32 v21, 0xffff0000, v21
	v_pk_add_f32 v[0:1], v[0:1], v[16:17]
	v_pk_add_f32 v[2:3], v[2:3], v[20:21]
	s_waitcnt vmcnt(10)
	v_lshlrev_b32_e32 v20, 16, v22
	v_and_b32_e32 v21, 0xffff0000, v22
	v_lshlrev_b32_e32 v22, 16, v23
	v_and_b32_e32 v23, 0xffff0000, v23
	v_pk_add_f32 v[0:1], v[0:1], v[20:21]
	v_pk_add_f32 v[2:3], v[2:3], v[22:23]
	s_waitcnt vmcnt(9)
	v_lshlrev_b32_e32 v20, 16, v24
	v_and_b32_e32 v21, 0xffff0000, v24
	v_lshlrev_b32_e32 v22, 16, v25
	v_and_b32_e32 v23, 0xffff0000, v25
	v_pk_add_f32 v[0:1], v[0:1], v[20:21]
	v_pk_add_f32 v[2:3], v[2:3], v[22:23]
	s_waitcnt vmcnt(8)
	v_lshlrev_b32_e32 v20, 16, v18
	v_and_b32_e32 v21, 0xffff0000, v18
	v_lshlrev_b32_e32 v18, 16, v19
	v_and_b32_e32 v19, 0xffff0000, v19
	v_pk_add_f32 v[0:1], v[0:1], v[20:21]
	v_pk_add_f32 v[2:3], v[2:3], v[18:19]
	s_waitcnt vmcnt(7)
	v_lshlrev_b32_e32 v16, 16, v30
	v_and_b32_e32 v17, 0xffff0000, v30
	v_lshlrev_b32_e32 v30, 16, v31
	v_and_b32_e32 v31, 0xffff0000, v31
	v_pk_add_f32 v[0:1], v[0:1], v[16:17]
	v_pk_add_f32 v[2:3], v[2:3], v[30:31]
	s_waitcnt vmcnt(6)
	v_lshlrev_b32_e32 v30, 16, v32
	v_and_b32_e32 v31, 0xffff0000, v32
	v_lshlrev_b32_e32 v32, 16, v33
	v_and_b32_e32 v33, 0xffff0000, v33
	v_pk_add_f32 v[0:1], v[0:1], v[30:31]
	v_pk_add_f32 v[2:3], v[2:3], v[32:33]
	s_waitcnt vmcnt(5)
	v_lshlrev_b32_e32 v30, 16, v34
	v_and_b32_e32 v31, 0xffff0000, v34
	v_lshlrev_b32_e32 v32, 16, v35
	v_and_b32_e32 v33, 0xffff0000, v35
	v_pk_add_f32 v[0:1], v[0:1], v[30:31]
	v_pk_add_f32 v[2:3], v[2:3], v[32:33]
	s_waitcnt vmcnt(4)
	v_lshlrev_b32_e32 v30, 16, v28
	v_and_b32_e32 v31, 0xffff0000, v28
	v_lshlrev_b32_e32 v28, 16, v29
	v_and_b32_e32 v29, 0xffff0000, v29
	v_pk_add_f32 v[0:1], v[0:1], v[30:31]
	v_pk_add_f32 v[2:3], v[2:3], v[28:29]
	s_waitcnt vmcnt(3)
	v_lshlrev_b32_e32 v16, 16, v208
	v_and_b32_e32 v17, 0xffff0000, v208
	v_lshlrev_b32_e32 v208, 16, v209
	v_and_b32_e32 v209, 0xffff0000, v209
	v_pk_add_f32 v[0:1], v[0:1], v[16:17]
	v_pk_add_f32 v[2:3], v[2:3], v[208:209]
	s_waitcnt vmcnt(2)
	v_lshlrev_b32_e32 v208, 16, v210
	v_and_b32_e32 v209, 0xffff0000, v210
	v_lshlrev_b32_e32 v210, 16, v211
	v_and_b32_e32 v211, 0xffff0000, v211
	v_pk_add_f32 v[0:1], v[0:1], v[208:209]
	v_pk_add_f32 v[2:3], v[2:3], v[210:211]
	s_waitcnt vmcnt(1)
	v_lshlrev_b32_e32 v208, 16, v212
	v_and_b32_e32 v209, 0xffff0000, v212
	v_lshlrev_b32_e32 v210, 16, v213
	v_and_b32_e32 v211, 0xffff0000, v213
	v_pk_add_f32 v[0:1], v[0:1], v[208:209]
	v_pk_add_f32 v[2:3], v[2:3], v[210:211]
	s_waitcnt vmcnt(0)
	v_lshlrev_b32_e32 v208, 16, v206
	v_and_b32_e32 v209, 0xffff0000, v206
	v_lshlrev_b32_e32 v206, 16, v207
	v_and_b32_e32 v207, 0xffff0000, v207
	v_pk_add_f32 v[0:1], v[0:1], v[208:209]
	v_pk_add_f32 v[2:3], v[2:3], v[206:207]
	s_cbranch_scc0 .LBB0_348
	v_lshlrev_b32_e32 v4, 4, v7
	v_lshlrev_b32_e32 v5, 9, v6
	s_movk_i32 s0, 0x80
	v_cmp_gt_i32_e32 vcc, s0, v106
	s_mov_b32 s57, 0
	v_add3_u32 v4, 0, v5, v4
	ds_write_b128 v4, v[0:3]
	s_waitcnt lgkmcnt(0)
	s_barrier
	s_and_saveexec_b64 s[8:9], vcc
	v_readlane_b32 s52, v254, 18
	v_readlane_b32 s66, v254, 21
	v_readlane_b32 s53, v254, 19
	v_readlane_b32 s67, v254, 20
	s_cbranch_execz .LBB0_351
	v_lshl_add_u32 v8, v106, 2, 0
	ds_read2st64_b32 v[0:1], v8 offset1:2
	ds_read2st64_b32 v[2:3], v8 offset0:4 offset1:6
	ds_read2st64_b32 v[6:7], v8 offset0:8 offset1:10
	s_lshl_b64 s[12:13], s[62:63], 9
	s_add_u32 s12, s54, s12
	s_waitcnt lgkmcnt(2)
	v_add_f32_e32 v0, 0, v0
	v_add_f32_e32 v0, v0, v1
	s_waitcnt lgkmcnt(1)
	v_add_f32_e32 v2, v0, v2
	ds_read2st64_b32 v[0:1], v8 offset0:12 offset1:14
	v_add_f32_e32 v2, v2, v3
	s_waitcnt lgkmcnt(1)
	v_add_f32_e32 v6, v2, v6
	ds_read2st64_b32 v[2:3], v8 offset0:16 offset1:18
	v_add_f32_e32 v6, v6, v7
	s_waitcnt lgkmcnt(1)
	v_add_f32_e32 v0, v6, v0
	v_add_f32_e32 v6, v0, v1
	ds_read2st64_b32 v[0:1], v8 offset0:20 offset1:22
	s_waitcnt lgkmcnt(1)
	v_add_f32_e32 v2, v6, v2
	ds_read2st64_b32 v[6:7], v8 offset0:24 offset1:26
	v_add_f32_e32 v9, v2, v3
	ds_read2st64_b32 v[2:3], v8 offset0:28 offset1:30
	s_waitcnt lgkmcnt(2)
	v_add_f32_e32 v0, v9, v0
	v_add_f32_e32 v0, v0, v1
	s_waitcnt lgkmcnt(1)
	v_add_f32_e32 v0, v0, v6
	v_add_f32_e32 v0, v0, v7
	s_addc_u32 s13, s55, s13
	v_ashrrev_i32_e32 v107, 31, v106
	s_waitcnt lgkmcnt(0)
	v_add_f32_e32 v0, v0, v2
	v_lshl_add_u64 v[4:5], v[106:107], 2, s[12:13]
	v_add_f32_e32 v0, v0, v3
	v_mul_f32_e32 v2, 0x3b800000, v0
	v_add_co_u32_e32 v0, vcc, 0x4a0000, v4
	s_nop 1
	v_addc_co_u32_e32 v1, vcc, 0, v5, vcc
	global_store_dword v[0:1], v2, off

.LBB0_1442:
	v_lshl_add_u64 v[8:9], v[4:5], 0, s[4:5]
	v_add_co_u32_e32 v10, vcc, 0x37c82000, v8
	s_add_u32 s4, s4, 0xd000
	s_nop 0
	v_addc_co_u32_e32 v11, vcc, 0, v9, vcc
	v_add_co_u32_e32 v12, vcc, s10, v8
	global_load_dwordx2 v[10:11], v[10:11], off offset:640
	s_nop 0
	v_addc_co_u32_e32 v13, vcc, 0, v9, vcc
	v_add_co_u32_e32 v14, vcc, s11, v8
	global_load_dwordx2 v[12:13], v[12:13], off offset:1664
	s_nop 0
	v_addc_co_u32_e32 v15, vcc, 0, v9, vcc
	v_add_co_u32_e32 v8, vcc, s14, v8
	global_load_dwordx2 v[14:15], v[14:15], off offset:2688
	s_nop 0
	v_addc_co_u32_e32 v9, vcc, 0, v9, vcc
	global_load_dwordx2 v[8:9], v[8:9], off offset:3712
	s_addc_u32 s5, s5, 0
	s_cmp_eq_u32 s4, 0x34000
	v_lshl_add_u64 v[18:19], v[4:5], 0, s[4:5]
	v_add_co_u32_e32 v20, vcc, 0x37c82000, v18
	s_add_u32 s4, s4, 0xd000
	s_nop 0
	v_addc_co_u32_e32 v21, vcc, 0, v19, vcc
	v_add_co_u32_e32 v22, vcc, s10, v18
	global_load_dwordx2 v[20:21], v[20:21], off offset:640
	s_nop 0
	v_addc_co_u32_e32 v23, vcc, 0, v19, vcc
	v_add_co_u32_e32 v24, vcc, s11, v18
	global_load_dwordx2 v[22:23], v[22:23], off offset:1664
	s_nop 0
	v_addc_co_u32_e32 v25, vcc, 0, v19, vcc
	v_add_co_u32_e32 v18, vcc, s14, v18
	global_load_dwordx2 v[24:25], v[24:25], off offset:2688
	s_nop 0
	v_addc_co_u32_e32 v19, vcc, 0, v19, vcc
	global_load_dwordx2 v[18:19], v[18:19], off offset:3712
	s_addc_u32 s5, s5, 0
	s_cmp_eq_u32 s4, 0x34000
	v_lshl_add_u64 v[28:29], v[4:5], 0, s[4:5]
	v_add_co_u32_e32 v30, vcc, 0x37c82000, v28
	s_add_u32 s4, s4, 0xd000
	s_nop 0
	v_addc_co_u32_e32 v31, vcc, 0, v29, vcc
	v_add_co_u32_e32 v32, vcc, s10, v28
	global_load_dwordx2 v[30:31], v[30:31], off offset:640
	s_nop 0
	v_addc_co_u32_e32 v33, vcc, 0, v29, vcc
	v_add_co_u32_e32 v34, vcc, s11, v28
	global_load_dwordx2 v[32:33], v[32:33], off offset:1664
	s_nop 0
	v_addc_co_u32_e32 v35, vcc, 0, v29, vcc
	v_add_co_u32_e32 v28, vcc, s14, v28
	global_load_dwordx2 v[34:35], v[34:35], off offset:2688
	s_nop 0
	v_addc_co_u32_e32 v29, vcc, 0, v29, vcc
	global_load_dwordx2 v[28:29], v[28:29], off offset:3712
	s_addc_u32 s5, s5, 0
	s_cmp_eq_u32 s4, 0x34000
	v_lshl_add_u64 v[206:207], v[4:5], 0, s[4:5]
	v_add_co_u32_e32 v208, vcc, 0x37c82000, v206
	s_add_u32 s4, s4, 0xd000
	s_nop 0
	v_addc_co_u32_e32 v209, vcc, 0, v207, vcc
	v_add_co_u32_e32 v210, vcc, s10, v206
	global_load_dwordx2 v[208:209], v[208:209], off offset:640
	s_nop 0
	v_addc_co_u32_e32 v211, vcc, 0, v207, vcc
	v_add_co_u32_e32 v212, vcc, s11, v206
	global_load_dwordx2 v[210:211], v[210:211], off offset:1664
	s_nop 0
	v_addc_co_u32_e32 v213, vcc, 0, v207, vcc
	v_add_co_u32_e32 v206, vcc, s14, v206
	global_load_dwordx2 v[212:213], v[212:213], off offset:2688
	s_nop 0
	v_addc_co_u32_e32 v207, vcc, 0, v207, vcc
	global_load_dwordx2 v[206:207], v[206:207], off offset:3712
	s_addc_u32 s5, s5, 0
	s_cmp_eq_u32 s4, 0x34000
	s_waitcnt vmcnt(15)
	v_lshlrev_b32_e32 v16, 16, v10
	v_and_b32_e32 v17, 0xffff0000, v10
	v_lshlrev_b32_e32 v10, 16, v11
	v_and_b32_e32 v11, 0xffff0000, v11
	v_pk_add_f32 v[0:1], v[0:1], v[16:17]
	v_pk_add_f32 v[2:3], v[2:3], v[10:11]
	s_waitcnt vmcnt(14)
	v_lshlrev_b32_e32 v10, 16, v12
	v_and_b32_e32 v11, 0xffff0000, v12
	v_lshlrev_b32_e32 v12, 16, v13
	v_and_b32_e32 v13, 0xffff0000, v13
	v_pk_add_f32 v[0:1], v[0:1], v[10:11]
	v_pk_add_f32 v[2:3], v[2:3], v[12:13]
	s_waitcnt vmcnt(13)
	v_lshlrev_b32_e32 v10, 16, v14
	v_and_b32_e32 v11, 0xffff0000, v14
	v_lshlrev_b32_e32 v12, 16, v15
	v_and_b32_e32 v13, 0xffff0000, v15
	v_pk_add_f32 v[0:1], v[0:1], v[10:11]
	v_pk_add_f32 v[2:3], v[2:3], v[12:13]
	s_waitcnt vmcnt(12)
	v_lshlrev_b32_e32 v10, 16, v8
	v_and_b32_e32 v11, 0xffff0000, v8
	v_lshlrev_b32_e32 v8, 16, v9
	v_and_b32_e32 v9, 0xffff0000, v9
	v_pk_add_f32 v[0:1], v[0:1], v[10:11]
	v_pk_add_f32 v[2:3], v[2:3], v[8:9]
	s_waitcnt vmcnt(11)
	v_lshlrev_b32_e32 v16, 16, v20
	v_and_b32_e32 v17, 0xffff0000, v20
	v_lshlrev_b32_e32 v20, 16, v21
	v_and_b32_e32 v21, 0xffff0000, v21
	v_pk_add_f32 v[0:1], v[0:1], v[16:17]
	v_pk_add_f32 v[2:3], v[2:3], v[20:21]
	s_waitcnt vmcnt(10)
	v_lshlrev_b32_e32 v20, 16, v22
	v_and_b32_e32 v21, 0xffff0000, v22
	v_lshlrev_b32_e32 v22, 16, v23
	v_and_b32_e32 v23, 0xffff0000, v23
	v_pk_add_f32 v[0:1], v[0:1], v[20:21]
	v_pk_add_f32 v[2:3], v[2:3], v[22:23]
	s_waitcnt vmcnt(9)
	v_lshlrev_b32_e32 v20, 16, v24
	v_and_b32_e32 v21, 0xffff0000, v24
	v_lshlrev_b32_e32 v22, 16, v25
	v_and_b32_e32 v23, 0xffff0000, v25
	v_pk_add_f32 v[0:1], v[0:1], v[20:21]
	v_pk_add_f32 v[2:3], v[2:3], v[22:23]
	s_waitcnt vmcnt(8)
	v_lshlrev_b32_e32 v20, 16, v18
	v_and_b32_e32 v21, 0xffff0000, v18
	v_lshlrev_b32_e32 v18, 16, v19
	v_and_b32_e32 v19, 0xffff0000, v19
	v_pk_add_f32 v[0:1], v[0:1], v[20:21]
	v_pk_add_f32 v[2:3], v[2:3], v[18:19]
	s_waitcnt vmcnt(7)
	v_lshlrev_b32_e32 v16, 16, v30
	v_and_b32_e32 v17, 0xffff0000, v30
	v_lshlrev_b32_e32 v30, 16, v31
	v_and_b32_e32 v31, 0xffff0000, v31
	v_pk_add_f32 v[0:1], v[0:1], v[16:17]
	v_pk_add_f32 v[2:3], v[2:3], v[30:31]
	s_waitcnt vmcnt(6)
	v_lshlrev_b32_e32 v30, 16, v32
	v_and_b32_e32 v31, 0xffff0000, v32
	v_lshlrev_b32_e32 v32, 16, v33
	v_and_b32_e32 v33, 0xffff0000, v33
	v_pk_add_f32 v[0:1], v[0:1], v[30:31]
	v_pk_add_f32 v[2:3], v[2:3], v[32:33]
	s_waitcnt vmcnt(5)
	v_lshlrev_b32_e32 v30, 16, v34
	v_and_b32_e32 v31, 0xffff0000, v34
	v_lshlrev_b32_e32 v32, 16, v35
	v_and_b32_e32 v33, 0xffff0000, v35
	v_pk_add_f32 v[0:1], v[0:1], v[30:31]
	v_pk_add_f32 v[2:3], v[2:3], v[32:33]
	s_waitcnt vmcnt(4)
	v_lshlrev_b32_e32 v30, 16, v28
	v_and_b32_e32 v31, 0xffff0000, v28
	v_lshlrev_b32_e32 v28, 16, v29
	v_and_b32_e32 v29, 0xffff0000, v29
	v_pk_add_f32 v[0:1], v[0:1], v[30:31]
	v_pk_add_f32 v[2:3], v[2:3], v[28:29]
	s_waitcnt vmcnt(3)
	v_lshlrev_b32_e32 v16, 16, v208
	v_and_b32_e32 v17, 0xffff0000, v208
	v_lshlrev_b32_e32 v208, 16, v209
	v_and_b32_e32 v209, 0xffff0000, v209
	v_pk_add_f32 v[0:1], v[0:1], v[16:17]
	v_pk_add_f32 v[2:3], v[2:3], v[208:209]
	s_waitcnt vmcnt(2)
	v_lshlrev_b32_e32 v208, 16, v210
	v_and_b32_e32 v209, 0xffff0000, v210
	v_lshlrev_b32_e32 v210, 16, v211
	v_and_b32_e32 v211, 0xffff0000, v211
	v_pk_add_f32 v[0:1], v[0:1], v[208:209]
	v_pk_add_f32 v[2:3], v[2:3], v[210:211]
	s_waitcnt vmcnt(1)
	v_lshlrev_b32_e32 v208, 16, v212
	v_and_b32_e32 v209, 0xffff0000, v212
	v_lshlrev_b32_e32 v210, 16, v213
	v_and_b32_e32 v211, 0xffff0000, v213
	v_pk_add_f32 v[0:1], v[0:1], v[208:209]
	v_pk_add_f32 v[2:3], v[2:3], v[210:211]
	s_waitcnt vmcnt(0)
	v_lshlrev_b32_e32 v208, 16, v206
	v_and_b32_e32 v209, 0xffff0000, v206
	v_lshlrev_b32_e32 v206, 16, v207
	v_and_b32_e32 v207, 0xffff0000, v207
	v_pk_add_f32 v[0:1], v[0:1], v[208:209]
	v_pk_add_f32 v[2:3], v[2:3], v[206:207]
	s_cbranch_scc0 .LBB0_1442
	v_lshlrev_b32_e32 v4, 4, v7
	v_lshlrev_b32_e32 v5, 9, v6
	s_movk_i32 s4, 0x80
	v_cmp_gt_i32_e32 vcc, s4, v106
	s_mov_b32 s5, 0
	v_add3_u32 v4, 0, v5, v4
	ds_write_b128 v4, v[0:3]
	s_waitcnt lgkmcnt(0)
	s_barrier
	s_and_saveexec_b64 s[10:11], vcc
	v_readlane_b32 s76, v254, 21
	v_readlane_b32 s77, v254, 20
	s_cbranch_execz .LBB0_1445
	v_lshl_add_u32 v8, v106, 2, 0
	ds_read2st64_b32 v[0:1], v8 offset1:2
	ds_read2st64_b32 v[2:3], v8 offset0:4 offset1:6
	ds_read2st64_b32 v[6:7], v8 offset0:8 offset1:10
	s_lshl_b64 s[14:15], s[78:79], 9
	s_add_u32 s14, s74, s14
	s_waitcnt lgkmcnt(2)
	v_add_f32_e32 v0, 0, v0
	v_add_f32_e32 v0, v0, v1
	s_waitcnt lgkmcnt(1)
	v_add_f32_e32 v2, v0, v2
	ds_read2st64_b32 v[0:1], v8 offset0:12 offset1:14
	v_add_f32_e32 v2, v2, v3
	s_waitcnt lgkmcnt(1)
	v_add_f32_e32 v6, v2, v6
	ds_read2st64_b32 v[2:3], v8 offset0:16 offset1:18
	v_add_f32_e32 v6, v6, v7
	s_waitcnt lgkmcnt(1)
	v_add_f32_e32 v0, v6, v0
	v_add_f32_e32 v6, v0, v1
	ds_read2st64_b32 v[0:1], v8 offset0:20 offset1:22
	s_waitcnt lgkmcnt(1)
	v_add_f32_e32 v2, v6, v2
	ds_read2st64_b32 v[6:7], v8 offset0:24 offset1:26
	v_add_f32_e32 v9, v2, v3
	ds_read2st64_b32 v[2:3], v8 offset0:28 offset1:30
	s_waitcnt lgkmcnt(2)
	v_add_f32_e32 v0, v9, v0
	v_add_f32_e32 v0, v0, v1
	s_waitcnt lgkmcnt(1)
	v_add_f32_e32 v0, v0, v6
	v_add_f32_e32 v0, v0, v7
	s_addc_u32 s15, s75, s15
	v_ashrrev_i32_e32 v107, 31, v106
	s_waitcnt lgkmcnt(0)
	v_add_f32_e32 v0, v0, v2
	v_lshl_add_u64 v[4:5], v[106:107], 2, s[14:15]
	v_add_f32_e32 v0, v0, v3
	v_mul_f32_e32 v2, 0x3b800000, v0
	v_add_co_u32_e32 v0, vcc, 0x4a0000, v4
	s_nop 1
	v_addc_co_u32_e32 v1, vcc, 0, v5, vcc
	global_store_dword v[0:1], v2, off
